# speedup vs baseline: 1.6649x; 1.0211x over previous
.LBB1_6:
	s_and_b32 s16, s2, 7
	s_mul_i32 s0, s16, 0x4b
	s_add_i32 s22, s3, s0
	s_lshr_b32 s23, s25, 6
	s_cmp_ge_u32 s23, s14
	s_cselect_b64 s[0:1], -1, 0
	s_cmp_lt_u32 s23, s15
	s_cselect_b64 s[2:3], -1, 0
	s_and_b64 s[8:9], s[0:1], s[2:3]
	s_mul_i32 s2, s22, 0x28000
	s_movk_i32 s0, 0xc0
	s_mul_hi_u32 s1, s22, 0x28000
	s_waitcnt lgkmcnt(0)
	s_add_u32 s2, s4, s2
	v_lshlrev_b32_e32 v1, 2, v0
	s_addc_u32 s3, s5, s1
	v_add_u32_e32 v2, 0x500, v1
	v_cmp_gt_u32_e64 s[0:1], s0, v0
	v_lshlrev_b32_e32 v104, 4, v0
	s_mul_i32 s16, s16, 5
	v_cndmask_b32_e64 v1, v1, v2, s[0:1]
	v_lshlrev_b32_e32 v2, 2, v1
	global_load_dwordx4 v[68:71], v104, s[2:3] nt
	s_and_saveexec_b64 s[44:45], s[0:1]
	global_load_dwordx4 v[64:67], v2, s[2:3] nt
	s_mov_b64 exec, s[44:45]
	s_add_i32 s24, s23, s16
	v_mov_b32_e32 v105, 0
	s_mul_i32 s4, s24, 20
	s_mov_b32 s5, 0
	v_mov_b32_e32 v3, v105
	v_lshrrev_b32_e32 v1, 4, v0
	s_lshl_b64 s[14:15], s[4:5], 12
	v_lshlrev_b32_e32 v6, 3, v0
	v_lshl_add_u64 v[96:97], s[2:3], 0, v[104:105]
	v_lshl_add_u64 v[98:99], s[2:3], 0, v[2:3]
	s_add_u32 s2, s6, s14
	v_and_b32_e32 v104, 0x3f0, v104
	s_addc_u32 s3, s7, s15
	v_lshl_add_u64 v[2:3], s[2:3], 0, v[104:105]
	s_mov_b64 s[14:15], 0x32000
	s_mov_b32 s4, 0x32000
	v_lshl_add_u64 v[100:101], v[2:3], 0, s[14:15]
	v_add_co_u32_e32 v2, vcc, s4, v2
	s_nop 1
	v_addc_co_u32_e32 v3, vcc, 0, v3, vcc
	s_and_saveexec_b64 s[44:45], s[8:9]
	global_load_dwordx4 v[80:83], v[100:101], off offset:1024
	global_load_dwordx4 v[88:91], v[100:101], off offset:2048
	global_load_dwordx4 v[92:95], v[2:3], off
	global_load_dwordx4 v[84:87], v[100:101], off offset:3072
	s_mov_b64 exec, s[44:45]
	s_movk_i32 s4, 0x2000
	v_add_co_u32_e32 v2, vcc, s4, v96
	s_nop 1
	v_addc_co_u32_e32 v3, vcc, 0, v97, vcc
	v_add_co_u32_e32 v4, vcc, s4, v98
	s_nop 1
	v_addc_co_u32_e32 v5, vcc, 0, v99, vcc
	global_load_dwordx4 v[76:79], v[2:3], off nt
	s_and_saveexec_b64 s[44:45], s[0:1]
	global_load_dwordx4 v[72:75], v[4:5], off nt
	s_mov_b64 exec, s[44:45]
	v_bfe_u32 v2, v0, 2, 4
	v_and_b32_e32 v0, 63, v0
	v_mul_u32_u24_e32 v2, 0xa0, v2
	v_lshlrev_b32_e32 v104, 4, v0
	v_and_or_b32 v108, v6, 24, v2
	v_mul_u32_u24_e32 v2, 0xa0, v1
	v_and_b32_e32 v3, 0x78, v6
	v_lshl_add_u64 v[0:1], s[2:3], 0, v[104:105]
	s_mov_b64 s[2:3], 0x33c00
	v_mov_b32_e32 v60, v105
	v_mov_b32_e32 v61, v105
	v_lshl_add_u64 v[102:103], v[0:1], 0, s[2:3]
	v_mov_b32_e32 v104, v105
	v_mov_b32_e32 v62, v105
	v_mov_b32_e32 v63, v105
	v_add_u32_e32 v109, v2, v3
	v_mov_b64_e32 v[56:57], v[60:61]
	v_mov_b64_e32 v[52:53], v[60:61]
	v_mov_b64_e32 v[48:49], v[60:61]
	v_mov_b64_e32 v[44:45], v[60:61]
	v_mov_b64_e32 v[40:41], v[60:61]
	v_mov_b64_e32 v[36:37], v[60:61]
	v_mov_b64_e32 v[32:33], v[60:61]
	v_mov_b64_e32 v[28:29], v[60:61]
	v_mov_b64_e32 v[24:25], v[60:61]
	v_mov_b64_e32 v[20:21], v[60:61]
	v_mov_b64_e32 v[16:17], v[60:61]
	v_mov_b64_e32 v[12:13], v[60:61]
	v_mov_b64_e32 v[8:9], v[60:61]
	v_mov_b64_e32 v[4:5], v[60:61]
	v_mov_b64_e32 v[0:1], v[60:61]
	s_mov_b64 s[14:15], 0x2000
	v_mov_b64_e32 v[58:59], v[62:63]
	v_mov_b64_e32 v[54:55], v[62:63]
	v_mov_b64_e32 v[50:51], v[62:63]
	v_mov_b64_e32 v[46:47], v[62:63]
	v_mov_b64_e32 v[42:43], v[62:63]
	v_mov_b64_e32 v[38:39], v[62:63]
	v_mov_b64_e32 v[34:35], v[62:63]
	v_mov_b64_e32 v[30:31], v[62:63]
	v_mov_b64_e32 v[26:27], v[62:63]
	v_mov_b64_e32 v[22:23], v[62:63]
	v_mov_b64_e32 v[18:19], v[62:63]
	v_mov_b64_e32 v[14:15], v[62:63]
	v_mov_b64_e32 v[10:11], v[62:63]
	v_mov_b64_e32 v[6:7], v[62:63]
	v_mov_b64_e32 v[2:3], v[62:63]
	s_mov_b32 s26, 0
	v_mov_b64_e32 v[106:107], v[104:105]

.LBB1_18:
	s_and_saveexec_b64 s[44:45], s[8:9]
	global_load_dwordx4 v[84:87], v[102:103], off offset:-3072
	global_load_dwordx4 v[88:91], v[102:103], off offset:-2048
	global_load_dwordx4 v[92:95], v[102:103], off offset:-1024
	global_load_dwordx4 v[80:83], v[102:103], off
	s_mov_b64 exec, s[44:45]
	s_add_i32 s27, s26, 2
	s_cmp_gt_u32 s26, 17
	s_cselect_b64 s[16:17], -1, 0
	s_cmp_lt_u32 s26, 18
	s_cselect_b64 s[18:19], -1, 0
	s_and_b64 s[20:21], s[18:19], exec
	s_cselect_b32 s4, s27, s26
	s_lshl_b32 s4, s4, 11
	s_lshl_b64 s[20:21], s[4:5], 2
	v_lshl_add_u64 v[64:65], v[96:97], 0, s[20:21]
	v_lshl_add_u64 v[66:67], v[98:99], 0, s[20:21]
	global_load_dwordx4 v[68:71], v[64:65], off nt
	s_nop 0
	s_and_saveexec_b64 s[44:45], s[0:1]
	global_load_dwordx4 v[64:67], v[66:67], off nt
	s_mov_b64 exec, s[44:45]
	s_waitcnt vmcnt(7)
	v_pk_fma_f32 v[104:105], v[76:77], v[76:77], v[104:105]
	v_pk_fma_f32 v[106:107], v[78:79], v[78:79], v[106:107]
	v_cvt_pk_f16_f32 v79, v78, v79
	v_cvt_pk_f16_f32 v78, v76, v77
	ds_write_b64 v109, v[78:79] offset:5120
	s_and_saveexec_b64 s[20:21], s[0:1]
	s_cbranch_execz .LBB1_20
	s_waitcnt vmcnt(6)
	v_pk_fma_f32 v[104:105], v[72:73], v[72:73], v[104:105]
	v_pk_fma_f32 v[106:107], v[74:75], v[74:75], v[106:107]
	v_cvt_pk_f16_f32 v75, v74, v75
	v_cvt_pk_f16_f32 v74, v72, v73
	ds_write_b64 v109, v[74:75] offset:8320

.LBB1_29:
	s_add_i32 s20, s26, 1
	s_and_b64 s[2:3], s[18:19], exec
	s_cselect_b32 s2, s27, s20
	s_lshl_b32 s4, s2, 12
	s_waitcnt vmcnt(6)
	v_lshl_add_u64 v[72:73], v[100:101], 0, s[4:5]
	s_and_saveexec_b64 s[44:45], s[8:9]
	global_load_dwordx4 v[92:95], v[72:73], off
	global_load_dwordx4 v[80:83], v[72:73], off offset:1024
	global_load_dwordx4 v[88:91], v[72:73], off offset:2048
	global_load_dwordx4 v[84:87], v[72:73], off offset:3072
	s_mov_b64 exec, s[44:45]
	s_add_i32 s2, s26, 3
	s_cmp_lt_u32 s26, 17
	s_cselect_b32 s2, s2, s20
	s_lshl_b32 s4, s2, 11
	s_lshl_b64 s[2:3], s[4:5], 2
	v_lshl_add_u64 v[72:73], v[96:97], 0, s[2:3]
	v_lshl_add_u64 v[74:75], v[98:99], 0, s[2:3]
	global_load_dwordx4 v[76:79], v[72:73], off nt
	s_nop 0
	s_and_saveexec_b64 s[44:45], s[0:1]
	global_load_dwordx4 v[72:75], v[74:75], off nt
	s_mov_b64 exec, s[44:45]
	v_lshl_add_u64 v[102:103], v[102:103], 0, s[14:15]
	s_and_b64 vcc, exec, s[16:17]
	s_cbranch_vccnz .LBB1_31
	s_mov_b32 s26, s27
	s_branch .LBB1_7

.Lsk_loop:
	s_nop 3
	v_add_f32_dpp v108, v72, v73 quad_perm:[0,1,2,3] row_mask:0x1 bank_mask:0xf
	v_add_f32_dpp v108, v76, v77 quad_perm:[0,1,2,3] row_mask:0x2 bank_mask:0xf
	v_add_f32_dpp v108, v80, v81 quad_perm:[0,1,2,3] row_mask:0x4 bank_mask:0xf
	v_add_f32_dpp v108, v84, v85 quad_perm:[0,1,2,3] row_mask:0x8 bank_mask:0xf
	v_rcp_f32_e32 v109, v108
	v_mov_b64_e32 v[88:89], s[32:33]
	v_mov_b64_e32 v[92:93], s[32:33]
	v_mul_f32_dpp v110, v109, v114 quad_perm:[0,2,0,2] row_mask:0xf bank_mask:0xf
	v_mul_f32_dpp v111, v109, v115 quad_perm:[1,3,1,3] row_mask:0xf bank_mask:0xf
	v_cvt_pk_bf16_f32 v68, v110, v111
	v_mov_b64_e32 v[96:97], s[32:33]
	v_mov_b64_e32 v[104:105], s[32:33]
	v_mov_b32_dpp v69, v68 row_ror:4 row_mask:0xf bank_mask:0xf
	v_mov_b32_dpp v70, v68 row_ror:8 row_mask:0xf bank_mask:0xf
	v_mov_b32_dpp v71, v68 row_ror:12 row_mask:0xf bank_mask:0xf
	s_nop 1
	v_smfmac_f32_16x16x64_bf16 v[88:91], v[68:71], v[32:39], v64
	v_smfmac_f32_16x16x64_bf16 v[92:95], v[68:71], v[40:47], v64
	v_smfmac_f32_16x16x64_bf16 v[96:99], v[68:71], v[48:55], v64
	v_smfmac_f32_16x16x64_bf16 v[104:107], v[68:71], v[56:63], v64
	s_nop 4
	v_add_f32_dpp v108, v88, v89 quad_perm:[0,1,2,3] row_mask:0x1 bank_mask:0xf
	v_add_f32_dpp v108, v92, v93 quad_perm:[0,1,2,3] row_mask:0x2 bank_mask:0xf
	v_add_f32_dpp v108, v96, v97 quad_perm:[0,1,2,3] row_mask:0x4 bank_mask:0xf
	v_add_f32_dpp v108, v104, v105 quad_perm:[0,1,2,3] row_mask:0x8 bank_mask:0xf
	v_rcp_f32_e32 v109, v108
	v_mov_b64_e32 v[72:73], s[32:33]
	v_mov_b64_e32 v[76:77], s[32:33]
	v_mul_f32_dpp v110, v109, v112 quad_perm:[0,2,0,2] row_mask:0xf bank_mask:0xf
	v_mul_f32_dpp v111, v109, v113 quad_perm:[1,3,1,3] row_mask:0xf bank_mask:0xf
	v_cvt_pk_bf16_f32 v68, v110, v111
	v_mov_b64_e32 v[80:81], s[32:33]
	v_mov_b64_e32 v[84:85], s[32:33]
	v_mov_b32_dpp v69, v68 row_ror:4 row_mask:0xf bank_mask:0xf
	v_mov_b32_dpp v70, v68 row_ror:8 row_mask:0xf bank_mask:0xf
	v_mov_b32_dpp v71, v68 row_ror:12 row_mask:0xf bank_mask:0xf
	v_cmp_ne_u32_e32 vcc, v68, v122
	v_mov_b32_e32 v122, v68
	s_cmp_eq_u64 vcc, 0
	s_cselect_b32 s30, 1, s30
	s_add_i32 s30, s30, -1
	s_cmp_lg_u32 s30, 0
	v_smfmac_f32_16x16x64_bf16 v[72:75], v[68:71], v[0:7], v64
	v_smfmac_f32_16x16x64_bf16 v[76:79], v[68:71], v[8:15], v64
	v_smfmac_f32_16x16x64_bf16 v[80:83], v[68:71], v[16:23], v64
	v_smfmac_f32_16x16x64_bf16 v[84:87], v[68:71], v[24:31], v64
	s_cbranch_scc1 .Lsk_loop
	s_nop 3
	v_add_f32_dpp v108, v72, v73 quad_perm:[0,1,2,3] row_mask:0x1 bank_mask:0xf
	v_add_f32_dpp v108, v76, v77 quad_perm:[0,1,2,3] row_mask:0x2 bank_mask:0xf
	v_add_f32_dpp v108, v80, v81 quad_perm:[0,1,2,3] row_mask:0x4 bank_mask:0xf
	v_add_f32_dpp v108, v84, v85 quad_perm:[0,1,2,3] row_mask:0x8 bank_mask:0xf
	v_rcp_f32_e32 v109, v108
	s_mov_b32 s34, 0x3d0df4e0
	s_mov_b32 s35, s34
	v_mul_f32_e32 v118, v117, v109
	v_lshlrev_b32_e32 v72, 16, v0
	v_and_b32_e32 v73, 0xffff0000, v0
	v_log_f32_e32 v74, v72
	v_log_f32_e32 v75, v73
	v_lshlrev_b32_e32 v76, 16, v1
	v_and_b32_e32 v77, 0xffff0000, v1
	v_log_f32_e32 v78, v76
	v_log_f32_e32 v79, v77
	v_pk_fma_f32 v[74:75], v[74:75], s[34:35], 1.0 op_sel_hi:[1,0,0]
	s_nop 0
	v_pk_fma_f32 v[78:79], v[78:79], s[34:35], 1.0 op_sel_hi:[1,0,0]
	v_pk_mul_f32 v[74:75], v[74:75], v[72:73]
	v_pk_mul_f32 v[78:79], v[78:79], v[76:77]
	v_cvt_pk_bf16_f32 v0, v74, v75
	v_cvt_pk_bf16_f32 v1, v78, v79
	v_lshlrev_b32_e32 v80, 16, v2
	v_and_b32_e32 v81, 0xffff0000, v2
	v_log_f32_e32 v82, v80
	v_log_f32_e32 v83, v81
	v_lshlrev_b32_e32 v84, 16, v3
	v_and_b32_e32 v85, 0xffff0000, v3
	v_log_f32_e32 v86, v84
	v_log_f32_e32 v87, v85
	v_pk_fma_f32 v[82:83], v[82:83], s[34:35], 1.0 op_sel_hi:[1,0,0]
	s_nop 0
	v_pk_fma_f32 v[86:87], v[86:87], s[34:35], 1.0 op_sel_hi:[1,0,0]
	v_pk_mul_f32 v[82:83], v[82:83], v[80:81]
	v_pk_mul_f32 v[86:87], v[86:87], v[84:85]
	v_cvt_pk_bf16_f32 v2, v82, v83
	v_cvt_pk_bf16_f32 v3, v86, v87
	v_lshlrev_b32_e32 v72, 16, v4
	v_and_b32_e32 v73, 0xffff0000, v4
	v_log_f32_e32 v74, v72
	v_log_f32_e32 v75, v73
	v_lshlrev_b32_e32 v76, 16, v5
	v_and_b32_e32 v77, 0xffff0000, v5
	v_log_f32_e32 v78, v76
	v_log_f32_e32 v79, v77
	v_pk_fma_f32 v[74:75], v[74:75], s[34:35], 1.0 op_sel_hi:[1,0,0]
	s_nop 0
	v_pk_fma_f32 v[78:79], v[78:79], s[34:35], 1.0 op_sel_hi:[1,0,0]
	v_pk_mul_f32 v[74:75], v[74:75], v[72:73]
	v_pk_mul_f32 v[78:79], v[78:79], v[76:77]
	v_cvt_pk_bf16_f32 v4, v74, v75
	v_cvt_pk_bf16_f32 v5, v78, v79
	v_lshlrev_b32_e32 v80, 16, v6
	v_and_b32_e32 v81, 0xffff0000, v6
	v_log_f32_e32 v82, v80
	v_log_f32_e32 v83, v81
	v_lshlrev_b32_e32 v84, 16, v7
	v_and_b32_e32 v85, 0xffff0000, v7
	v_log_f32_e32 v86, v84
	v_log_f32_e32 v87, v85
	v_pk_fma_f32 v[82:83], v[82:83], s[34:35], 1.0 op_sel_hi:[1,0,0]
	s_nop 0
	v_pk_fma_f32 v[86:87], v[86:87], s[34:35], 1.0 op_sel_hi:[1,0,0]
	v_pk_mul_f32 v[82:83], v[82:83], v[80:81]
	v_pk_mul_f32 v[86:87], v[86:87], v[84:85]
	v_cvt_pk_bf16_f32 v6, v82, v83
	v_cvt_pk_bf16_f32 v7, v86, v87
	v_lshlrev_b32_e32 v72, 16, v8
	v_and_b32_e32 v73, 0xffff0000, v8
	v_log_f32_e32 v74, v72
	v_log_f32_e32 v75, v73
	v_lshlrev_b32_e32 v76, 16, v9
	v_and_b32_e32 v77, 0xffff0000, v9
	v_log_f32_e32 v78, v76
	v_log_f32_e32 v79, v77
	v_pk_fma_f32 v[74:75], v[74:75], s[34:35], 1.0 op_sel_hi:[1,0,0]
	s_nop 0
	v_pk_fma_f32 v[78:79], v[78:79], s[34:35], 1.0 op_sel_hi:[1,0,0]
	v_pk_mul_f32 v[74:75], v[74:75], v[72:73]
	v_pk_mul_f32 v[78:79], v[78:79], v[76:77]
	v_cvt_pk_bf16_f32 v8, v74, v75
	v_cvt_pk_bf16_f32 v9, v78, v79
	v_lshlrev_b32_e32 v80, 16, v10
	v_and_b32_e32 v81, 0xffff0000, v10
	v_log_f32_e32 v82, v80
	v_log_f32_e32 v83, v81
	v_lshlrev_b32_e32 v84, 16, v11
	v_and_b32_e32 v85, 0xffff0000, v11
	v_log_f32_e32 v86, v84
	v_log_f32_e32 v87, v85
	v_pk_fma_f32 v[82:83], v[82:83], s[34:35], 1.0 op_sel_hi:[1,0,0]
	s_nop 0
	v_pk_fma_f32 v[86:87], v[86:87], s[34:35], 1.0 op_sel_hi:[1,0,0]
	v_pk_mul_f32 v[82:83], v[82:83], v[80:81]
	v_pk_mul_f32 v[86:87], v[86:87], v[84:85]
	v_cvt_pk_bf16_f32 v10, v82, v83
	v_cvt_pk_bf16_f32 v11, v86, v87
	v_lshlrev_b32_e32 v72, 16, v12
	v_and_b32_e32 v73, 0xffff0000, v12
	v_log_f32_e32 v74, v72
	v_log_f32_e32 v75, v73
	v_lshlrev_b32_e32 v76, 16, v13
	v_and_b32_e32 v77, 0xffff0000, v13
	v_log_f32_e32 v78, v76
	v_log_f32_e32 v79, v77
	v_pk_fma_f32 v[74:75], v[74:75], s[34:35], 1.0 op_sel_hi:[1,0,0]
	s_nop 0
	v_pk_fma_f32 v[78:79], v[78:79], s[34:35], 1.0 op_sel_hi:[1,0,0]
	v_pk_mul_f32 v[74:75], v[74:75], v[72:73]
	v_pk_mul_f32 v[78:79], v[78:79], v[76:77]
	v_cvt_pk_bf16_f32 v12, v74, v75
	v_cvt_pk_bf16_f32 v13, v78, v79
	v_lshlrev_b32_e32 v80, 16, v14
	v_and_b32_e32 v81, 0xffff0000, v14
	v_log_f32_e32 v82, v80
	v_log_f32_e32 v83, v81
	v_lshlrev_b32_e32 v84, 16, v15
	v_and_b32_e32 v85, 0xffff0000, v15
	v_log_f32_e32 v86, v84
	v_log_f32_e32 v87, v85
	v_pk_fma_f32 v[82:83], v[82:83], s[34:35], 1.0 op_sel_hi:[1,0,0]
	s_nop 0
	v_pk_fma_f32 v[86:87], v[86:87], s[34:35], 1.0 op_sel_hi:[1,0,0]
	v_pk_mul_f32 v[82:83], v[82:83], v[80:81]
	v_pk_mul_f32 v[86:87], v[86:87], v[84:85]
	v_cvt_pk_bf16_f32 v14, v82, v83
	v_cvt_pk_bf16_f32 v15, v86, v87
	v_lshlrev_b32_e32 v72, 16, v16
	v_and_b32_e32 v73, 0xffff0000, v16
	v_log_f32_e32 v74, v72
	v_log_f32_e32 v75, v73
	v_lshlrev_b32_e32 v76, 16, v17
	v_and_b32_e32 v77, 0xffff0000, v17
	v_log_f32_e32 v78, v76
	v_log_f32_e32 v79, v77
	v_pk_fma_f32 v[74:75], v[74:75], s[34:35], 1.0 op_sel_hi:[1,0,0]
	s_nop 0
	v_pk_fma_f32 v[78:79], v[78:79], s[34:35], 1.0 op_sel_hi:[1,0,0]
	v_pk_mul_f32 v[74:75], v[74:75], v[72:73]
	v_pk_mul_f32 v[78:79], v[78:79], v[76:77]
	v_cvt_pk_bf16_f32 v16, v74, v75
	v_cvt_pk_bf16_f32 v17, v78, v79
	v_lshlrev_b32_e32 v80, 16, v18
	v_and_b32_e32 v81, 0xffff0000, v18
	v_log_f32_e32 v82, v80
	v_log_f32_e32 v83, v81
	v_lshlrev_b32_e32 v84, 16, v19
	v_and_b32_e32 v85, 0xffff0000, v19
	v_log_f32_e32 v86, v84
	v_log_f32_e32 v87, v85
	v_pk_fma_f32 v[82:83], v[82:83], s[34:35], 1.0 op_sel_hi:[1,0,0]
	s_nop 0
	v_pk_fma_f32 v[86:87], v[86:87], s[34:35], 1.0 op_sel_hi:[1,0,0]
	v_pk_mul_f32 v[82:83], v[82:83], v[80:81]
	v_pk_mul_f32 v[86:87], v[86:87], v[84:85]
	v_cvt_pk_bf16_f32 v18, v82, v83
	v_cvt_pk_bf16_f32 v19, v86, v87
	v_lshlrev_b32_e32 v72, 16, v20
	v_and_b32_e32 v73, 0xffff0000, v20
	v_log_f32_e32 v74, v72
	v_log_f32_e32 v75, v73
	v_lshlrev_b32_e32 v76, 16, v21
	v_and_b32_e32 v77, 0xffff0000, v21
	v_log_f32_e32 v78, v76
	v_log_f32_e32 v79, v77
	v_pk_fma_f32 v[74:75], v[74:75], s[34:35], 1.0 op_sel_hi:[1,0,0]
	s_nop 0
	v_pk_fma_f32 v[78:79], v[78:79], s[34:35], 1.0 op_sel_hi:[1,0,0]
	v_pk_mul_f32 v[74:75], v[74:75], v[72:73]
	v_pk_mul_f32 v[78:79], v[78:79], v[76:77]
	v_cvt_pk_bf16_f32 v20, v74, v75
	v_cvt_pk_bf16_f32 v21, v78, v79
	v_lshlrev_b32_e32 v80, 16, v22
	v_and_b32_e32 v81, 0xffff0000, v22
	v_log_f32_e32 v82, v80
	v_log_f32_e32 v83, v81
	v_lshlrev_b32_e32 v84, 16, v23
	v_and_b32_e32 v85, 0xffff0000, v23
	v_log_f32_e32 v86, v84
	v_log_f32_e32 v87, v85
	v_pk_fma_f32 v[82:83], v[82:83], s[34:35], 1.0 op_sel_hi:[1,0,0]
	s_nop 0
	v_pk_fma_f32 v[86:87], v[86:87], s[34:35], 1.0 op_sel_hi:[1,0,0]
	v_pk_mul_f32 v[82:83], v[82:83], v[80:81]
	v_pk_mul_f32 v[86:87], v[86:87], v[84:85]
	v_cvt_pk_bf16_f32 v22, v82, v83
	v_cvt_pk_bf16_f32 v23, v86, v87
	v_lshlrev_b32_e32 v72, 16, v24
	v_and_b32_e32 v73, 0xffff0000, v24
	v_log_f32_e32 v74, v72
	v_log_f32_e32 v75, v73
	v_lshlrev_b32_e32 v76, 16, v25
	v_and_b32_e32 v77, 0xffff0000, v25
	v_log_f32_e32 v78, v76
	v_log_f32_e32 v79, v77
	v_pk_fma_f32 v[74:75], v[74:75], s[34:35], 1.0 op_sel_hi:[1,0,0]
	s_nop 0
	v_pk_fma_f32 v[78:79], v[78:79], s[34:35], 1.0 op_sel_hi:[1,0,0]
	v_pk_mul_f32 v[74:75], v[74:75], v[72:73]
	v_pk_mul_f32 v[78:79], v[78:79], v[76:77]
	v_cvt_pk_bf16_f32 v24, v74, v75
	v_cvt_pk_bf16_f32 v25, v78, v79
	v_lshlrev_b32_e32 v80, 16, v26
	v_and_b32_e32 v81, 0xffff0000, v26
	v_log_f32_e32 v82, v80
	v_log_f32_e32 v83, v81
	v_lshlrev_b32_e32 v84, 16, v27
	v_and_b32_e32 v85, 0xffff0000, v27
	v_log_f32_e32 v86, v84
	v_log_f32_e32 v87, v85
	v_pk_fma_f32 v[82:83], v[82:83], s[34:35], 1.0 op_sel_hi:[1,0,0]
	s_nop 0
	v_pk_fma_f32 v[86:87], v[86:87], s[34:35], 1.0 op_sel_hi:[1,0,0]
	v_pk_mul_f32 v[82:83], v[82:83], v[80:81]
	v_pk_mul_f32 v[86:87], v[86:87], v[84:85]
	v_cvt_pk_bf16_f32 v26, v82, v83
	v_cvt_pk_bf16_f32 v27, v86, v87
	v_lshlrev_b32_e32 v72, 16, v28
	v_and_b32_e32 v73, 0xffff0000, v28
	v_log_f32_e32 v74, v72
	v_log_f32_e32 v75, v73
	v_lshlrev_b32_e32 v76, 16, v29
	v_and_b32_e32 v77, 0xffff0000, v29
	v_log_f32_e32 v78, v76
	v_log_f32_e32 v79, v77
	v_pk_fma_f32 v[74:75], v[74:75], s[34:35], 1.0 op_sel_hi:[1,0,0]
	s_nop 0
	v_pk_fma_f32 v[78:79], v[78:79], s[34:35], 1.0 op_sel_hi:[1,0,0]
	v_pk_mul_f32 v[74:75], v[74:75], v[72:73]
	v_pk_mul_f32 v[78:79], v[78:79], v[76:77]
	v_cvt_pk_bf16_f32 v28, v74, v75
	v_cvt_pk_bf16_f32 v29, v78, v79
	v_lshlrev_b32_e32 v80, 16, v30
	v_and_b32_e32 v81, 0xffff0000, v30
	v_log_f32_e32 v82, v80
	v_log_f32_e32 v83, v81
	v_lshlrev_b32_e32 v84, 16, v31
	v_and_b32_e32 v85, 0xffff0000, v31
	v_log_f32_e32 v86, v84
	v_log_f32_e32 v87, v85
	v_pk_fma_f32 v[82:83], v[82:83], s[34:35], 1.0 op_sel_hi:[1,0,0]
	s_nop 0
	v_pk_fma_f32 v[86:87], v[86:87], s[34:35], 1.0 op_sel_hi:[1,0,0]
	v_pk_mul_f32 v[82:83], v[82:83], v[80:81]
	v_pk_mul_f32 v[86:87], v[86:87], v[84:85]
	v_cvt_pk_bf16_f32 v30, v82, v83
	v_cvt_pk_bf16_f32 v31, v86, v87
	v_mov_b64_e32 v[88:89], s[32:33]
	v_mov_b64_e32 v[92:93], s[32:33]
	v_mov_b64_e32 v[96:97], s[32:33]
	v_mov_b64_e32 v[104:105], s[32:33]
	s_nop 1
	v_smfmac_f32_16x16x64_bf16 v[88:91], v[68:71], v[0:7], v64
	v_smfmac_f32_16x16x64_bf16 v[92:95], v[68:71], v[8:15], v64
	v_smfmac_f32_16x16x64_bf16 v[96:99], v[68:71], v[16:23], v64
	v_smfmac_f32_16x16x64_bf16 v[104:107], v[68:71], v[24:31], v64
	s_nop 4
	v_add_f32_dpp v108, v88, v89 quad_perm:[0,1,2,3] row_mask:0x1 bank_mask:0xf
	v_add_f32_dpp v108, v92, v93 quad_perm:[0,1,2,3] row_mask:0x2 bank_mask:0xf
	v_add_f32_dpp v108, v96, v97 quad_perm:[0,1,2,3] row_mask:0x4 bank_mask:0xf
	v_add_f32_dpp v108, v104, v105 quad_perm:[0,1,2,3] row_mask:0x8 bank_mask:0xf
	v_add_f32_e32 v108, 0xab8cbccc, v108
	v_mul_f32_e32 v108, v118, v108
	s_nop 1
	v_add_f32_dpp v108, v108, v108 row_ror:8 row_mask:0xf bank_mask:0xf
	s_nop 1
	v_add_f32_dpp v108, v108, v108 row_ror:4 row_mask:0xf bank_mask:0xf
	s_nop 1
	v_add_f32_dpp v108, v108, v108 row_ror:2 row_mask:0xf bank_mask:0xf
	s_nop 1
	v_add_f32_dpp v108, v108, v108 row_ror:1 row_mask:0xf bank_mask:0xf
	s_nop 1
	v_mov_b32_e32 v109, v108
	s_nop 1
	v_permlane16_swap_b32_e32 v108, v109
	v_add_f32_e32 v108, v108, v109
	v_mov_b32_e32 v109, v108
	s_nop 1
	v_permlane32_swap_b32_e32 v108, v109
	v_add_f32_e32 v108, v108, v109
	v_cmp_eq_u32_e32 vcc, 0, v100
	s_and_saveexec_b64 s[0:1], vcc
	s_cbranch_execz .LBB1_38
	s_mul_i32 s0, s22, 5
	s_add_i32 s0, s0, s23
	s_mov_b32 s1, 0
	s_lshl_b64 s[0:1], s[0:1], 2
	s_add_u32 s0, s12, s0
	s_addc_u32 s1, s13, s1
	v_mov_b32_e32 v109, 0
	global_store_dword v109, v108, s[0:1]
